# expert-weight conversion ring: counted vmcnt across the per-tile barrier instead of hipcc's vmcnt(0) drain (3 tiles really in flight)
# speedup vs baseline: 1.0087x; 1.0087x over previous
.LBB0_161:
	v_and_b32_e32 v11, 3, v1
	v_ashrrev_i32_e32 v12, 2, v1
	v_lshlrev_b32_e32 v10, 4, v11
	v_lshlrev_b32_e32 v13, 13, v11
	v_lshlrev_b32_e32 v11, 3, v11
	s_mov_b32 s0, 0x3ffffffc
	v_bitop3_b32 v11, v11, v12, s0 bitop3:0x78
	v_and_or_b32 v11, v12, 3, v11
	s_add_u32 s16, s2, 0x22800000
	v_lshlrev_b32_e32 v11, 2, v11
	s_addc_u32 s17, s3, 0
	v_add3_u32 v14, 0, v13, v11
	v_ashrrev_i32_e32 v13, 31, v12
	s_add_u32 s18, s2, 0x2800000
	s_mov_b32 s1, 0
	v_lshlrev_b64 v[12:13], 11, v[12:13]
	v_mov_b32_e32 v11, 0
	s_addc_u32 s19, s3, 0
	s_mov_b32 s20, 1
	s_mov_b32 s21, 0xc3e00000
	s_mov_b32 s22, 0xc000
	v_mov_b32_e32 v15, 0x43e00000
	s_mov_b32 s23, s15
	s_waitcnt vmcnt(0)
	s_branch .LBB0_165

.LBB0_174:
	s_add_i32 s0, s20, -1
	s_and_b32 s26, s0, 3
	s_add_i32 s0, s26, s15
	s_mul_hi_i32 s8, s0, 0x2aaaaaab
	s_lshr_b32 s9, s8, 31
	s_ashr_i32 s8, s8, 8
	s_add_i32 s10, s8, s9
	s_mul_i32 s8, s10, 0xfffffa00
	s_add_i32 s8, s8, s0
	s_ashr_i32 s27, s8, 9
	s_and_b32 s33, s0, 15
	s_ashr_i32 s11, s10, 31
	s_cmp_gt_i32 s27, 1
	s_mov_b64 s[12:13], -1
	s_waitcnt lgkmcnt(0)
	s_barrier
	s_cbranch_scc0 .LBB0_176
	s_lshl_b32 s12, s33, 18
	s_lshl_b64 s[8:9], s[10:11], 22
	s_add_u32 s8, s16, s8
	s_addc_u32 s9, s17, s9
	s_add_u32 s8, s8, s12
	s_addc_u32 s9, s9, 0
	s_mov_b64 s[12:13], 0

.LBB0_294:
	v_and_b32_e32 v11, 3, v1
	v_ashrrev_i32_e32 v12, 2, v1
	v_lshlrev_b32_e32 v10, 4, v11
	v_lshlrev_b32_e32 v13, 13, v11
	v_lshlrev_b32_e32 v11, 3, v11
	s_mov_b32 s0, 0x3ffffffc
	v_bitop3_b32 v11, v11, v12, s0 bitop3:0x78
	v_and_or_b32 v11, v12, 3, v11
	s_add_u32 s14, s2, 0x22800000
	v_lshlrev_b32_e32 v11, 2, v11
	s_addc_u32 s15, s3, 0
	s_add_u32 s16, s2, 0x2800000
	v_add3_u32 v14, 0, v13, v11
	v_ashrrev_i32_e32 v13, 31, v12
	s_addc_u32 s17, s3, 0
	s_mov_b32 s1, 0
	v_lshlrev_b64 v[12:13], 11, v[12:13]
	v_mov_b32_e32 v11, 0
	s_mov_b32 s18, 1
	s_mov_b32 s19, 0xc3e00000
	s_mov_b32 s20, 0xc000
	v_mov_b32_e32 v15, 0x43e00000
	s_mov_b32 s21, s13
	s_waitcnt vmcnt(0)
	s_branch .LBB0_298

.LBB0_305:
	s_add_i32 s0, s18, -1
	s_and_b32 s24, s0, 3
	s_add_i32 s0, s24, s13
	s_mul_hi_i32 s6, s0, 0x2aaaaaab
	s_lshr_b32 s7, s6, 31
	s_ashr_i32 s6, s6, 8
	s_add_i32 s8, s6, s7
	s_mul_i32 s6, s8, 0xfffffa00
	s_add_i32 s6, s6, s0
	s_ashr_i32 s25, s6, 9
	s_and_b32 s26, s0, 15
	s_ashr_i32 s9, s8, 31
	s_cmp_gt_i32 s25, 1
	s_mov_b64 s[10:11], -1
	s_waitcnt lgkmcnt(0)
	s_barrier
	s_cbranch_scc0 .LBB0_307
	s_lshl_b32 s10, s26, 18
	s_lshl_b64 s[6:7], s[8:9], 22
	s_add_u32 s6, s14, s6
	s_addc_u32 s7, s15, s7
	s_add_u32 s6, s6, s10
	s_addc_u32 s7, s7, 0
	s_mov_b64 s[10:11], 0

.LBB0_681:
	v_and_b32_e32 v11, 3, v1
	v_ashrrev_i32_e32 v12, 2, v1
	v_lshlrev_b32_e32 v10, 4, v11
	v_lshlrev_b32_e32 v13, 13, v11
	v_lshlrev_b32_e32 v11, 3, v11
	s_mov_b32 s0, 0x3ffffffc
	v_bitop3_b32 v11, v11, v12, s0 bitop3:0x78
	v_and_or_b32 v11, v12, 3, v11
	s_add_u32 s18, s2, 0x22800000
	v_lshlrev_b32_e32 v11, 2, v11
	s_addc_u32 s19, s3, 0
	v_add3_u32 v14, 0, v13, v11
	v_ashrrev_i32_e32 v13, 31, v12
	s_add_u32 s20, s2, 0x2800000
	s_mov_b32 s1, 0
	v_lshlrev_b64 v[12:13], 11, v[12:13]
	v_mov_b32_e32 v11, 0
	s_addc_u32 s21, s3, 0
	s_mov_b32 s22, 1
	s_mov_b32 s23, 0xc3e00000
	s_mov_b32 s24, 0xc000
	v_mov_b32_e32 v15, 0x43e00000
	s_mov_b32 s25, s17
	s_waitcnt vmcnt(0)
	s_branch .LBB0_685

.LBB0_692:
	s_add_i32 s0, s22, -1
	s_and_b32 s28, s0, 3
	s_add_i32 s0, s28, s17
	s_mul_hi_i32 s8, s0, 0x2aaaaaab
	s_lshr_b32 s9, s8, 31
	s_ashr_i32 s8, s8, 8
	s_add_i32 s12, s8, s9
	s_mul_i32 s8, s12, 0xfffffa00
	s_add_i32 s8, s8, s0
	s_ashr_i32 s29, s8, 9
	s_and_b32 s30, s0, 15
	s_ashr_i32 s13, s12, 31
	s_cmp_gt_i32 s29, 1
	s_mov_b64 s[14:15], -1
	s_waitcnt lgkmcnt(0)
	s_barrier
	s_cbranch_scc0 .LBB0_694
	s_lshl_b32 s14, s30, 18
	s_lshl_b64 s[8:9], s[12:13], 22
	s_add_u32 s8, s18, s8
	s_addc_u32 s9, s19, s9
	s_add_u32 s8, s8, s14
	s_addc_u32 s9, s9, 0
	s_mov_b64 s[14:15], 0
